# attention: static priority raise moved to the younger half (waves 4..7) - strategy 4
# speedup vs baseline: 1.0064x; 1.0018x over previous
; template <bool FIRST>
; __device__ __forceinline__ bool partialSM(f32x16& p0, f32x16& p1, float& M, f32x16& minit, float& alpha) {
;     float tmax = p0[0]; for (int r = 1; r < 16; ++r) tmax = fmaxf(tmax, p0[r]); for (int r = 0; r < 16; ++r) tmax = fmaxf(tmax, p1[r]);
;     { auto rr = __builtin_amdgcn_permlane32_swap(__float_as_uint(tmax), __float_as_uint(tmax), false, false);
;       tmax = fmaxf(__uint_as_float(rr[0]), __uint_as_float(rr[1])); }
;     const float d0 = tmax - PLOG2;
;     const bool moved = FIRST || !__all(d0 <= THR * 1.4426950408889634f);
; template <int AV>
; __device__ __forceinline__ void block(const BlockRef& cur, const BlockRef& nxt, char* lds, Seam& S, const int wid, const QNorm& QN) {
;     ...
;     if (wid < 4) __builtin_amdgcn_s_setprio(1);
.LBB0_515:
	s_nop 15
	s_nop 0
	v_max_f32_e32 v32, v1, v1
	v_max_f32_e32 v33, v0, v0
	v_max_f32_e32 v32, v33, v32
	v_max3_f32 v32, v32, v2, v3
	v_max3_f32 v32, v32, v4, v5
	v_max3_f32 v32, v32, v6, v7
	v_max3_f32 v32, v32, v8, v9
	v_max3_f32 v32, v32, v10, v11
	v_max3_f32 v32, v32, v12, v13
	v_max3_f32 v32, v32, v14, v15
	v_max3_f32 v32, v32, v16, v17
	v_max3_f32 v32, v32, v18, v19
	v_max3_f32 v32, v32, v20, v21
	v_max3_f32 v32, v32, v22, v23
	v_max3_f32 v32, v32, v24, v25
	v_max3_f32 v32, v32, v26, v27
	v_max3_f32 v32, v32, v28, v29
	v_max3_f32 v32, v32, v30, v31
	v_mov_b32_e32 v33, v32
	s_and_b64 vcc, exec, s[4:5]
	s_nop 0
	v_permlane32_swap_b32_e32 v32, v33
	s_cbranch_vccz .LBB0_517
	s_setprio 1

; __device__ __forceinline__ void qnorm_rope(const u32x2 (&q)[12], const QCoef& C, i32x8 (&qf)[3]) {
;     float sn = 0.f, sp = 0.f, v[8];
; #pragma unroll
;     for (int f = 0; f < 8; ++f) { unpk8(q[f], v);
; #pragma unroll
;         for (int e = 0; e < 8; ++e) sn += v[e] * v[e]; }
; #pragma unroll
;     for (int f = 8; f < 12; ++f) { unpk8(q[f], v);
; #pragma unroll
;         for (int e = 0; e < 8; ++e) sp += v[e] * v[e]; }
;     { auto rr = __builtin_amdgcn_permlane32_swap(__float_as_uint(sn), __float_as_uint(sn), false, false); sn = __uint_as_float(rr[0]) + __uint_as_float(rr[1]); }
;     { auto rr = __builtin_amdgcn_permlane32_swap(__float_as_uint(sp), __float_as_uint(sp), false, false); sp = __uint_as_float(rr[0]) + __uint_as_float(rr[1]); }
.LBB0_582:
	s_waitcnt vmcnt(27)
	v_cvt_pk_f32_fp8_e32 v[174:175], v86
	v_cvt_pk_f32_fp8_sdwa v[168:169], v86 src0_sel:WORD_1
	v_lshlrev_b32_e32 v89, 2, v188
	v_cvt_pk_f32_fp8_e32 v[172:173], v87
	v_mul_f32_e32 v86, v175, v175
	v_and_b32_e32 v88, 32, v188
	v_and_b32_e32 v90, 48, v89
	v_lshlrev_b32_e32 v194, 6, v198
	v_cvt_pk_f32_fp8_sdwa v[166:167], v87 src0_sel:WORD_1
	v_pk_fma_f32 v[86:87], v[174:175], v[174:175], v[86:87] op_sel_hi:[1,1,0]
	v_bitop3_b32 v193, v89, v88, 48 bitop3:0x6c
	v_bitop3_b32 v192, v90, v194, v88 bitop3:0xde
	v_pk_fma_f32 v[86:87], v[168:169], v[168:169], v[86:87]
	v_mul_f32_e32 v88, v169, v169
	v_pk_add_f32 v[86:87], v[88:89], v[86:87] op_sel_hi:[0,1]
	v_pk_fma_f32 v[86:87], v[172:173], v[172:173], v[86:87]
	v_mul_f32_e32 v88, v173, v173
	s_waitcnt vmcnt(26)
	v_cvt_pk_f32_fp8_e32 v[170:171], v84
	v_pk_add_f32 v[86:87], v[88:89], v[86:87] op_sel_hi:[0,1]
	v_pk_fma_f32 v[86:87], v[166:167], v[166:167], v[86:87]
	v_mul_f32_e32 v88, v167, v167
	v_cvt_pk_f32_fp8_sdwa v[162:163], v84 src0_sel:WORD_1
	v_pk_add_f32 v[86:87], v[88:89], v[86:87] op_sel_hi:[0,1]
	v_cvt_pk_f32_fp8_e32 v[164:165], v85
	v_cvt_pk_f32_fp8_sdwa v[160:161], v85 src0_sel:WORD_1
	v_pk_fma_f32 v[84:85], v[170:171], v[170:171], v[86:87]
	v_mul_f32_e32 v86, v171, v171
	v_pk_add_f32 v[84:85], v[86:87], v[84:85] op_sel_hi:[0,1]
	v_pk_fma_f32 v[84:85], v[162:163], v[162:163], v[84:85]
	v_mul_f32_e32 v86, v163, v163
	v_pk_add_f32 v[84:85], v[86:87], v[84:85] op_sel_hi:[0,1]
	v_pk_fma_f32 v[84:85], v[164:165], v[164:165], v[84:85]
	v_mul_f32_e32 v86, v165, v165
	s_waitcnt vmcnt(25)
	v_cvt_pk_f32_fp8_e32 v[142:143], v82
	v_pk_add_f32 v[84:85], v[86:87], v[84:85] op_sel_hi:[0,1]
	v_pk_fma_f32 v[84:85], v[160:161], v[160:161], v[84:85]
	v_mul_f32_e32 v86, v161, v161
	v_cvt_pk_f32_fp8_sdwa v[138:139], v82 src0_sel:WORD_1
	v_pk_add_f32 v[84:85], v[86:87], v[84:85] op_sel_hi:[0,1]
	v_cvt_pk_f32_fp8_e32 v[140:141], v83
	v_cvt_pk_f32_fp8_sdwa v[136:137], v83 src0_sel:WORD_1
	v_pk_fma_f32 v[82:83], v[142:143], v[142:143], v[84:85]
	v_mul_f32_e32 v84, v143, v143
	v_pk_add_f32 v[82:83], v[84:85], v[82:83] op_sel_hi:[0,1]
	v_pk_fma_f32 v[82:83], v[138:139], v[138:139], v[82:83]
	v_mul_f32_e32 v84, v139, v139
	v_pk_add_f32 v[82:83], v[84:85], v[82:83] op_sel_hi:[0,1]
	v_pk_fma_f32 v[82:83], v[140:141], v[140:141], v[82:83]
	v_mul_f32_e32 v84, v141, v141
	s_waitcnt vmcnt(24)
	v_cvt_pk_f32_fp8_e32 v[134:135], v80
	v_pk_add_f32 v[82:83], v[84:85], v[82:83] op_sel_hi:[0,1]
	v_pk_fma_f32 v[82:83], v[136:137], v[136:137], v[82:83]
	v_mul_f32_e32 v84, v137, v137
	v_cvt_pk_f32_fp8_sdwa v[130:131], v80 src0_sel:WORD_1
	v_pk_add_f32 v[82:83], v[84:85], v[82:83] op_sel_hi:[0,1]
	v_cvt_pk_f32_fp8_e32 v[132:133], v81
	v_cvt_pk_f32_fp8_sdwa v[128:129], v81 src0_sel:WORD_1
	v_pk_fma_f32 v[80:81], v[134:135], v[134:135], v[82:83]
	v_mul_f32_e32 v82, v135, v135
	v_pk_add_f32 v[80:81], v[82:83], v[80:81] op_sel_hi:[0,1]
	v_pk_fma_f32 v[80:81], v[130:131], v[130:131], v[80:81]
	v_mul_f32_e32 v82, v131, v131
	v_pk_add_f32 v[80:81], v[82:83], v[80:81] op_sel_hi:[0,1]
	v_pk_fma_f32 v[80:81], v[132:133], v[132:133], v[80:81]
	v_mul_f32_e32 v82, v133, v133
	s_waitcnt vmcnt(23)
	v_cvt_pk_f32_fp8_e32 v[126:127], v78
	v_pk_add_f32 v[80:81], v[82:83], v[80:81] op_sel_hi:[0,1]
	v_pk_fma_f32 v[80:81], v[128:129], v[128:129], v[80:81]
	v_mul_f32_e32 v82, v129, v129
	v_cvt_pk_f32_fp8_sdwa v[122:123], v78 src0_sel:WORD_1
	v_pk_add_f32 v[80:81], v[82:83], v[80:81] op_sel_hi:[0,1]
	v_cvt_pk_f32_fp8_e32 v[124:125], v79
	v_cvt_pk_f32_fp8_sdwa v[120:121], v79 src0_sel:WORD_1
	v_pk_fma_f32 v[78:79], v[126:127], v[126:127], v[80:81]
	v_mul_f32_e32 v80, v127, v127
	v_pk_add_f32 v[78:79], v[80:81], v[78:79] op_sel_hi:[0,1]
	v_pk_fma_f32 v[78:79], v[122:123], v[122:123], v[78:79]
	v_mul_f32_e32 v80, v123, v123
	v_pk_add_f32 v[78:79], v[80:81], v[78:79] op_sel_hi:[0,1]
	v_pk_fma_f32 v[78:79], v[124:125], v[124:125], v[78:79]
	v_mul_f32_e32 v80, v125, v125
	s_waitcnt vmcnt(22)
	v_cvt_pk_f32_fp8_e32 v[118:119], v76
	v_pk_add_f32 v[78:79], v[80:81], v[78:79] op_sel_hi:[0,1]
	v_pk_fma_f32 v[78:79], v[120:121], v[120:121], v[78:79]
	v_mul_f32_e32 v80, v121, v121
	v_cvt_pk_f32_fp8_sdwa v[114:115], v76 src0_sel:WORD_1
	v_pk_add_f32 v[78:79], v[80:81], v[78:79] op_sel_hi:[0,1]
	v_cvt_pk_f32_fp8_e32 v[116:117], v77
	v_cvt_pk_f32_fp8_sdwa v[112:113], v77 src0_sel:WORD_1
	v_pk_fma_f32 v[76:77], v[118:119], v[118:119], v[78:79]
	v_mul_f32_e32 v78, v119, v119
	v_pk_add_f32 v[76:77], v[78:79], v[76:77] op_sel_hi:[0,1]
	v_pk_fma_f32 v[76:77], v[114:115], v[114:115], v[76:77]
	v_mul_f32_e32 v78, v115, v115
	v_pk_add_f32 v[76:77], v[78:79], v[76:77] op_sel_hi:[0,1]
	v_pk_fma_f32 v[76:77], v[116:117], v[116:117], v[76:77]
	v_mul_f32_e32 v78, v117, v117
	s_waitcnt vmcnt(21)
	v_cvt_pk_f32_fp8_e32 v[110:111], v74
	v_pk_add_f32 v[76:77], v[78:79], v[76:77] op_sel_hi:[0,1]
	v_pk_fma_f32 v[76:77], v[112:113], v[112:113], v[76:77]
	v_mul_f32_e32 v78, v113, v113
	v_cvt_pk_f32_fp8_sdwa v[106:107], v74 src0_sel:WORD_1
	s_waitcnt vmcnt(19)
; __device__ __forceinline__ void qnorm_rope(const u32x2 (&q)[12], const QCoef& C, i32x8 (&qf)[3]) {
;     ...
;     for (int f = 0; f < 8; ++f) { unpk8(q[f], v);
; #pragma unroll
;         for (int e = 0; e < 8; ++e) sn += v[e] * v[e]; }
; #pragma unroll
;     for (int f = 8; f < 12; ++f) { unpk8(q[f], v);
; #pragma unroll
;         for (int e = 0; e < 8; ++e) sp += v[e] * v[e]; }
;     { auto rr = __builtin_amdgcn_permlane32_swap(__float_as_uint(sn), __float_as_uint(sn), false, false); sn = __uint_as_float(rr[0]) + __uint_as_float(rr[1]); }
;     { auto rr = __builtin_amdgcn_permlane32_swap(__float_as_uint(sp), __float_as_uint(sp), false, false); sp = __uint_as_float(rr[0]) + __uint_as_float(rr[1]); }
;     const float rn = rsqrtf(sn * (1.f / 128.f) + RMS_EPS), rp = rsqrtf(sp * (1.f / 64.f) + RMS_EPS);
	v_cvt_pk_f32_fp8_e32 v[90:91], v66
	v_pk_add_f32 v[76:77], v[78:79], v[76:77] op_sel_hi:[0,1]
	v_cvt_pk_f32_fp8_e32 v[108:109], v75
	v_cvt_pk_f32_fp8_sdwa v[104:105], v75 src0_sel:WORD_1
	v_pk_fma_f32 v[74:75], v[110:111], v[110:111], v[76:77]
	v_mul_f32_e32 v76, v111, v111
	v_cvt_pk_f32_fp8_sdwa v[86:87], v66 src0_sel:WORD_1
	v_pk_add_f32 v[74:75], v[76:77], v[74:75] op_sel_hi:[0,1]
	v_pk_fma_f32 v[74:75], v[106:107], v[106:107], v[74:75]
	v_mul_f32_e32 v76, v107, v107
	v_cvt_pk_f32_fp8_e32 v[82:83], v67
	v_mul_f32_e32 v66, v91, v91
	v_pk_add_f32 v[74:75], v[76:77], v[74:75] op_sel_hi:[0,1]
	v_cvt_pk_f32_fp8_sdwa v[80:81], v67 src0_sel:WORD_1
	v_pk_fma_f32 v[66:67], v[90:91], v[90:91], v[66:67] op_sel_hi:[1,1,0]
	v_pk_fma_f32 v[74:75], v[108:109], v[108:109], v[74:75]
	v_mul_f32_e32 v76, v109, v109
	v_cvt_pk_f32_fp8_e32 v[102:103], v70
	v_cvt_pk_f32_fp8_sdwa v[98:99], v70 src0_sel:WORD_1
	v_pk_fma_f32 v[66:67], v[86:87], v[86:87], v[66:67]
	v_mul_f32_e32 v70, v87, v87
	v_pk_add_f32 v[74:75], v[76:77], v[74:75] op_sel_hi:[0,1]
	v_pk_add_f32 v[66:67], v[70:71], v[66:67] op_sel_hi:[0,1]
	v_pk_fma_f32 v[74:75], v[104:105], v[104:105], v[74:75]
	v_mul_f32_e32 v76, v105, v105
	v_pk_fma_f32 v[66:67], v[82:83], v[82:83], v[66:67]
	v_mul_f32_e32 v70, v83, v83
	v_pk_add_f32 v[176:177], v[76:77], v[74:75] op_sel_hi:[0,1]
	v_pk_add_f32 v[66:67], v[70:71], v[66:67] op_sel_hi:[0,1]
	s_waitcnt vmcnt(18)
	v_cvt_pk_f32_fp8_e32 v[74:75], v64
	v_pk_fma_f32 v[66:67], v[80:81], v[80:81], v[66:67]
	v_mul_f32_e32 v70, v81, v81
	v_cvt_pk_f32_fp8_e32 v[100:101], v71
	v_cvt_pk_f32_fp8_sdwa v[96:97], v71 src0_sel:WORD_1
	v_pk_add_f32 v[76:77], v[70:71], v[66:67] op_sel_hi:[0,1]
	v_cvt_pk_f32_fp8_sdwa v[70:71], v64 src0_sel:WORD_1
	v_cvt_pk_f32_fp8_e32 v[66:67], v65
	v_pk_fma_f32 v[76:77], v[74:75], v[74:75], v[76:77]
	v_mul_f32_e32 v78, v75, v75
	v_pk_add_f32 v[76:77], v[78:79], v[76:77] op_sel_hi:[0,1]
	v_cvt_pk_f32_fp8_sdwa v[64:65], v65 src0_sel:WORD_1
	v_pk_fma_f32 v[76:77], v[70:71], v[70:71], v[76:77]
	v_mul_f32_e32 v78, v71, v71
	v_pk_add_f32 v[76:77], v[78:79], v[76:77] op_sel_hi:[0,1]
	v_pk_fma_f32 v[76:77], v[66:67], v[66:67], v[76:77]
	v_mul_f32_e32 v78, v67, v67
	s_waitcnt vmcnt(17)
	v_cvt_pk_f32_fp8_e32 v[94:95], v72
	v_pk_add_f32 v[76:77], v[78:79], v[76:77] op_sel_hi:[0,1]
	v_pk_fma_f32 v[76:77], v[64:65], v[64:65], v[76:77]
	v_mul_f32_e32 v78, v65, v65
	v_cvt_pk_f32_fp8_sdwa v[92:93], v72 src0_sel:WORD_1
	v_pk_add_f32 v[76:77], v[78:79], v[76:77] op_sel_hi:[0,1]
	v_cvt_pk_f32_fp8_e32 v[88:89], v73
	v_cvt_pk_f32_fp8_sdwa v[84:85], v73 src0_sel:WORD_1
	v_pk_fma_f32 v[72:73], v[94:95], v[94:95], v[76:77]
	v_mul_f32_e32 v76, v95, v95
	v_pk_add_f32 v[72:73], v[76:77], v[72:73] op_sel_hi:[0,1]
	v_pk_fma_f32 v[72:73], v[92:93], v[92:93], v[72:73]
	v_mul_f32_e32 v76, v93, v93
	v_pk_add_f32 v[72:73], v[76:77], v[72:73] op_sel_hi:[0,1]
	v_pk_fma_f32 v[72:73], v[88:89], v[88:89], v[72:73]
	v_mul_f32_e32 v76, v89, v89
	v_pk_add_f32 v[72:73], v[76:77], v[72:73] op_sel_hi:[0,1]
	s_waitcnt vmcnt(16)
	v_cvt_pk_f32_fp8_e32 v[78:79], v68
	v_pk_fma_f32 v[72:73], v[84:85], v[84:85], v[72:73]
	v_mul_f32_e32 v76, v85, v85
	v_pk_add_f32 v[178:179], v[76:77], v[72:73] op_sel_hi:[0,1]
	v_cvt_pk_f32_fp8_sdwa v[76:77], v68 src0_sel:WORD_1
	v_cvt_pk_f32_fp8_e32 v[72:73], v69
	v_pk_fma_f32 v[178:179], v[78:79], v[78:79], v[178:179]
	v_mul_f32_e32 v180, v79, v79
	v_pk_add_f32 v[178:179], v[180:181], v[178:179] op_sel_hi:[0,1]
	v_cvt_pk_f32_fp8_sdwa v[68:69], v69 src0_sel:WORD_1
	v_pk_fma_f32 v[178:179], v[76:77], v[76:77], v[178:179]
	v_mul_f32_e32 v180, v77, v77
	v_pk_add_f32 v[178:179], v[180:181], v[178:179] op_sel_hi:[0,1]
	v_pk_fma_f32 v[178:179], v[72:73], v[72:73], v[178:179]
	v_mul_f32_e32 v180, v73, v73
	v_pk_add_f32 v[178:179], v[180:181], v[178:179] op_sel_hi:[0,1]
	v_pk_fma_f32 v[178:179], v[68:69], v[68:69], v[178:179]
	v_mul_f32_e32 v180, v69, v69
	v_pk_add_f32 v[178:179], v[180:181], v[178:179] op_sel_hi:[0,1]
	v_pk_fma_f32 v[176:177], v[102:103], v[102:103], v[176:177]
	v_mul_f32_e32 v180, v103, v103
	v_pk_add_f32 v[176:177], v[180:181], v[176:177] op_sel_hi:[0,1]
	v_pk_fma_f32 v[176:177], v[98:99], v[98:99], v[176:177]
	v_mul_f32_e32 v180, v99, v99
	v_pk_add_f32 v[176:177], v[180:181], v[176:177] op_sel_hi:[0,1]
	v_pk_fma_f32 v[176:177], v[100:101], v[100:101], v[176:177]
	v_mul_f32_e32 v180, v101, v101
	v_pk_add_f32 v[176:177], v[180:181], v[176:177] op_sel_hi:[0,1]
	v_pk_fma_f32 v[176:177], v[96:97], v[96:97], v[176:177]
	v_mul_f32_e32 v180, v97, v97
	v_pk_add_f32 v[176:177], v[180:181], v[176:177] op_sel_hi:[0,1]
	v_mov_b32_e32 v181, v176
	s_nop 1
	v_permlane32_swap_b32_e32 v176, v181
	v_mov_b32_e32 v180, v178
	s_nop 1
	v_permlane32_swap_b32_e32 v178, v180
	v_mov_b32_e32 v179, v176
	s_mov_b32 s6, 0x3c800000
	v_pk_add_f32 v[176:177], v[178:179], v[180:181]
	s_brev_b32 s7, 60
	v_pk_fma_f32 v[176:177], v[176:177], s[6:7], v[186:187] op_sel_hi:[1,1,0]
	s_nop 0
	v_mul_f32_e32 v178, 0x4b800000, v177
	v_cmp_gt_f32_e64 s[6:7], s30, v177
	v_cmp_gt_f32_e32 vcc, s30, v176
	s_nop 0
	v_cndmask_b32_e64 v177, v177, v178, s[6:7]
	v_rsq_f32_e32 v177, v177
	s_nop 0
	v_mul_f32_e32 v178, 0x45800000, v177
	v_cndmask_b32_e64 v177, v177, v178, s[6:7]
	v_mul_f32_e32 v178, 0x4b800000, v176
	v_cndmask_b32_e32 v176, v176, v178, vcc
	v_mul_f32_e32 v182, 0x3e800000, v177
	v_rsq_f32_e32 v196, v176
	v_mul_f32_e32 v174, v174, v182
	v_mul_f32_e32 v175, v175, v182
	v_mul_f32_e32 v176, v168, v182
	v_mul_f32_e32 v177, v167, v182
	v_mul_f32_e32 v169, v169, v182
	v_cvt_pk_fp8_f32 v168, v174, v175
	v_mul_f32_e32 v172, v172, v182
	v_mul_f32_e32 v173, v173, v182
	v_mul_f32_e32 v166, v166, v182
; __device__ __forceinline__ unsigned cvt_pk4_fp8(float a, float b, float c, float d) { int w; asm("" : "=v"(w));     w = __builtin_amdgcn_cvt_pk_fp8_f32(a, b, w, false); w = __builtin_amdgcn_cvt_pk_fp8_f32(c, d, w, true); return (unsigned)w; }
; __device__ __forceinline__ void qnorm_rope(const u32x2 (&q)[12], const QCoef& C, i32x8 (&qf)[3]) {
;     ...
;     const float rn = rsqrtf(sn * (1.f / 128.f) + RMS_EPS), rp = rsqrtf(sp * (1.f / 64.f) + RMS_EPS);
; #pragma unroll
;     for (int f = 0; f < 8; ++f) { unpk8(q[f], v);
; #pragma unroll
;         for (int e = 0; e < 8; ++e) v[e] *= rn * QSC;
;         qf[f >> 2][2 * (f & 3)] = (int)cvt_pk4_fp8(v[0], v[1], v[2], v[3]); qf[f >> 2][2 * (f & 3) + 1] = (int)cvt_pk4_fp8(v[4], v[5], v[6], v[7]); }
; #pragma unroll
;     for (int f = 0; f < 2; ++f) {
;         float t1[8], t2[8], o1[8], o2[8]; unpk8(q[8 + f], t1); unpk8(q[10 + f], t2);
; #pragma unroll
;         for (int e = 0; e < 8; ++e) { const int j = 2 * f + (e >> 2), k = e & 3; const float a = t1[e] * (rp * QSC) * C.ga[j][k], b = t2[e] * (rp * QSC) * C.gb[j][k]; o1[e] = a * C.c[j][k] - b * C.s[j][k]; o2[e] = b * C.c[j][k] + a * C.s[j][k]; }
;         qf[2][2 * f] = (int)cvt_pk4_fp8(o1[0], o1[1], o1[2], o1[3]); qf[2][2 * f + 1] = (int)cvt_pk4_fp8(o1[4], o1[5], o1[6], o1[7]);
;         qf[2][4 + 2 * f] = (int)cvt_pk4_fp8(o2[0], o2[1], o2[2], o2[3]); qf[2][5 + 2 * f] = (int)cvt_pk4_fp8(o2[4], o2[5], o2[6], o2[7]); }
	v_cvt_pk_fp8_f32 v168, v176, v169 op_sel:[0,0,1]
	v_cvt_pk_fp8_f32 v169, v172, v173
	v_mul_f32_e32 v100, v100, v182
	v_mul_f32_e32 v101, v101, v182
	v_cvt_pk_fp8_f32 v169, v166, v177 op_sel:[0,0,1]
	v_mul_f32_e32 v166, v170, v182
	v_mul_f32_e32 v171, v171, v182
	v_mul_f32_e32 v162, v162, v182
	v_mul_f32_e32 v163, v163, v182
	v_mul_f32_e32 v164, v164, v182
	v_mul_f32_e32 v165, v165, v182
	v_mul_f32_e32 v160, v160, v182
	v_mul_f32_e32 v161, v161, v182
	v_mul_f32_e32 v142, v142, v182
	v_mul_f32_e32 v143, v143, v182
	v_mul_f32_e32 v138, v138, v182
	v_mul_f32_e32 v139, v139, v182
	v_mul_f32_e32 v140, v140, v182
	v_mul_f32_e32 v141, v141, v182
	v_mul_f32_e32 v136, v136, v182
	v_mul_f32_e32 v137, v137, v182
	v_mul_f32_e32 v134, v134, v182
	v_mul_f32_e32 v135, v135, v182
	v_mul_f32_e32 v130, v130, v182
	v_mul_f32_e32 v131, v131, v182
	v_mul_f32_e32 v132, v132, v182
	v_mul_f32_e32 v133, v133, v182
	v_mul_f32_e32 v128, v128, v182
	v_mul_f32_e32 v129, v129, v182
	v_mul_f32_e32 v126, v126, v182
	v_mul_f32_e32 v127, v127, v182
	v_mul_f32_e32 v122, v122, v182
	v_mul_f32_e32 v123, v123, v182
	v_mul_f32_e32 v124, v124, v182
	v_mul_f32_e32 v125, v125, v182
	v_mul_f32_e32 v120, v120, v182
	v_mul_f32_e32 v121, v121, v182
	v_mul_f32_e32 v118, v118, v182
	v_mul_f32_e32 v119, v119, v182
	v_mul_f32_e32 v114, v114, v182
	v_mul_f32_e32 v115, v115, v182
	v_mul_f32_e32 v116, v116, v182
	v_mul_f32_e32 v117, v117, v182
	v_mul_f32_e32 v112, v112, v182
	v_mul_f32_e32 v113, v113, v182
	v_mul_f32_e32 v110, v110, v182
	v_mul_f32_e32 v111, v111, v182
	v_mul_f32_e32 v106, v106, v182
	v_mul_f32_e32 v107, v107, v182
	v_mul_f32_e32 v108, v108, v182
	v_mul_f32_e32 v109, v109, v182
	v_mul_f32_e32 v104, v104, v182
	v_mul_f32_e32 v105, v105, v182
	v_mul_f32_e32 v102, v102, v182
	v_mul_f32_e32 v103, v103, v182
	v_mul_f32_e32 v98, v98, v182
	v_mul_f32_e32 v99, v99, v182
	v_mul_f32_e32 v96, v96, v182
	v_mul_f32_e32 v97, v97, v182
	v_cvt_pk_fp8_f32 v183, v100, v101
	v_cvt_pk_fp8_f32 v182, v102, v103
	v_mul_f32_e32 v197, 0x45800000, v196
	s_waitcnt vmcnt(8)
	v_mov_b32_e32 v100, v60
	v_cvt_pk_fp8_f32 v183, v96, v97 op_sel:[0,0,1]
	v_cndmask_b32_e32 v96, v196, v197, vcc
	v_cvt_pk_fp8_f32 v182, v98, v99 op_sel:[0,0,1]
	v_mul_f32_e32 v96, 0x3e800000, v96
	v_mov_b32_e32 v98, v94
	v_mov_b32_e32 v99, v90
	v_pk_mul_f32 v[98:99], v[98:99], v[96:97] op_sel_hi:[1,0]
	v_mov_b32_e32 v101, v56
	v_pk_mul_f32 v[98:99], v[100:101], v[98:99]
	v_mov_b32_e32 v100, v52
	v_mov_b32_e32 v101, v48
	v_pk_mul_f32 v[100:101], v[100:101], v[98:99]
	v_mov_b32_e32 v90, v95
	v_sub_f32_e32 v94, v101, v100
	v_mov_b32_e32 v100, v48
	v_mov_b32_e32 v101, v52
	v_pk_mul_f32 v[98:99], v[100:101], v[98:99]
	v_mov_b32_e32 v56, v61
	v_add_f32_e32 v97, v98, v99
	v_pk_mul_f32 v[90:91], v[90:91], v[96:97] op_sel_hi:[1,0]
	v_mov_b32_e32 v48, v53
	v_pk_mul_f32 v[56:57], v[56:57], v[90:91]
	v_mov_b32_e32 v52, v49
	v_pk_mul_f32 v[60:61], v[48:49], v[56:57]
	v_pk_mul_f32 v[48:49], v[52:53], v[56:57]
	v_mov_b32_e32 v52, v62
	v_add_f32_e32 v56, v48, v49
	v_mov_b32_e32 v48, v92
	v_mov_b32_e32 v49, v86
	v_pk_mul_f32 v[48:49], v[48:49], v[96:97] op_sel_hi:[1,0]
	v_mov_b32_e32 v53, v58
	v_pk_mul_f32 v[48:49], v[52:53], v[48:49]
	v_mov_b32_e32 v52, v54
	v_mov_b32_e32 v53, v50
	v_pk_mul_f32 v[52:53], v[52:53], v[48:49]
	v_mov_b32_e32 v86, v93
	v_sub_f32_e32 v57, v53, v52
	v_mov_b32_e32 v52, v50
	v_mov_b32_e32 v53, v54
	v_pk_mul_f32 v[48:49], v[52:53], v[48:49]
	v_sub_f32_e32 v60, v61, v60
	v_add_f32_e32 v61, v48, v49
	v_pk_mul_f32 v[48:49], v[86:87], v[96:97] op_sel_hi:[1,0]
	v_mov_b32_e32 v58, v63
	v_pk_mul_f32 v[48:49], v[58:59], v[48:49]
	v_mov_b32_e32 v50, v55
	v_mov_b32_e32 v54, v51
	v_pk_mul_f32 v[52:53], v[50:51], v[48:49]
	v_pk_mul_f32 v[48:49], v[54:55], v[48:49]
	v_sub_f32_e32 v52, v53, v52
	v_add_f32_e32 v53, v48, v49
	v_mov_b32_e32 v48, v88
	v_mov_b32_e32 v49, v82
	v_pk_mul_f32 v[48:49], v[48:49], v[96:97] op_sel_hi:[1,0]
	v_mov_b32_e32 v50, v44
	v_mov_b32_e32 v51, v40
	v_pk_mul_f32 v[48:49], v[50:51], v[48:49]
	v_mov_b32_e32 v50, v36
	v_mov_b32_e32 v51, v32
	v_pk_mul_f32 v[50:51], v[50:51], v[48:49]
	v_mov_b32_e32 v82, v89
	v_sub_f32_e32 v54, v51, v50
	v_mov_b32_e32 v50, v32
	v_mov_b32_e32 v51, v36
	v_pk_mul_f32 v[48:49], v[50:51], v[48:49]
	v_mov_b32_e32 v40, v45
	v_add_f32_e32 v50, v48, v49
	v_pk_mul_f32 v[48:49], v[82:83], v[96:97] op_sel_hi:[1,0]
	v_mov_b32_e32 v32, v37
	v_pk_mul_f32 v[40:41], v[40:41], v[48:49]
	v_mov_b32_e32 v36, v33
	v_pk_mul_f32 v[44:45], v[32:33], v[40:41]
	v_pk_mul_f32 v[32:33], v[36:37], v[40:41]
	v_add_f32_e32 v40, v32, v33
	v_mov_b32_e32 v32, v84
	v_mov_b32_e32 v33, v80
	v_cvt_pk_fp8_f32 v170, v166, v171
	v_pk_mul_f32 v[32:33], v[32:33], v[96:97] op_sel_hi:[1,0]
	v_mov_b32_e32 v36, v46
	v_mov_b32_e32 v37, v42
	v_cvt_pk_fp8_f32 v171, v164, v165
	v_pk_mul_f32 v[32:33], v[36:37], v[32:33]
	v_mov_b32_e32 v36, v38
	v_mov_b32_e32 v37, v34
	v_pk_mul_f32 v[36:37], v[36:37], v[32:33]
	v_mov_b32_e32 v80, v85
	v_sub_f32_e32 v41, v37, v36
	v_mov_b32_e32 v36, v34
	v_mov_b32_e32 v37, v38
	v_pk_mul_f32 v[32:33], v[36:37], v[32:33]
	v_cvt_pk_fp8_f32 v171, v160, v161 op_sel:[0,0,1]
	v_sub_f32_e32 v44, v45, v44
	v_add_f32_e32 v45, v32, v33
	v_pk_mul_f32 v[32:33], v[80:81], v[96:97] op_sel_hi:[1,0]
	v_mov_b32_e32 v42, v47
	v_cvt_pk_fp8_f32 v165, v50, v40
	v_pk_mul_f32 v[32:33], v[42:43], v[32:33]
	v_mov_b32_e32 v34, v39
	v_mov_b32_e32 v38, v35
	v_cvt_pk_fp8_f32 v161, v54, v44
	v_pk_mul_f32 v[36:37], v[34:35], v[32:33]
	v_pk_mul_f32 v[32:33], v[38:39], v[32:33]
	v_sub_f32_e32 v34, v37, v36
	v_add_f32_e32 v32, v32, v33
	v_cvt_pk_fp8_f32 v165, v45, v32 op_sel:[0,0,1]
	v_mov_b32_e32 v32, v78
	v_mov_b32_e32 v33, v74
	v_cvt_pk_fp8_f32 v161, v41, v34 op_sel:[0,0,1]
	v_pk_mul_f32 v[32:33], v[32:33], v[96:97] op_sel_hi:[1,0]
	s_waitcnt vmcnt(0)
; __device__ __forceinline__ unsigned cvt_pk4_fp8(float a, float b, float c, float d) { int w; asm("" : "=v"(w));     w = __builtin_amdgcn_cvt_pk_fp8_f32(a, b, w, false); w = __builtin_amdgcn_cvt_pk_fp8_f32(c, d, w, true); return (unsigned)w; }
; __device__ __forceinline__ void qkt(f32x16& p0, f32x16& p1, const char* stg, int ka, const i32x8* qf, const f32x16& minit) {
;     p0 = minit; p1 = minit;
; #pragma unroll
;     for (int s = 0; s < 3; ++s) { const char* a = stg + SOFF_K + s * 4096 + ka; const char* b = stg + SOFF_K + s * 4096 + (ka ^ 16);
;         const i32x4 a0 = *reinterpret_cast<const i32x4*>(a), a1 = *reinterpret_cast<const i32x4*>(b);
;         const i32x4 c0 = *reinterpret_cast<const i32x4*>(a + 2048), c1 = *reinterpret_cast<const i32x4*>(b + 2048);
;         p0 = __builtin_amdgcn_mfma_scale_f32_32x32x64_f8f6f4(__builtin_shufflevector(a0, a1, 0, 1, 2, 3, 4, 5, 6, 7), qf[s], p0, 0, 0, 0, 0, 0, 0);
;         p1 = __builtin_amdgcn_mfma_scale_f32_32x32x64_f8f6f4(__builtin_shufflevector(c0, c1, 0, 1, 2, 3, 4, 5, 6, 7), qf[s], p1, 0, 0, 0, 0, 0, 0); }
; }
; __device__ __forceinline__ void qnorm_rope(const u32x2 (&q)[12], const QCoef& C, i32x8 (&qf)[3]) {
;     ...
;     for (int f = 0; f < 2; ++f) {
;         float t1[8], t2[8], o1[8], o2[8]; unpk8(q[8 + f], t1); unpk8(q[10 + f], t2);
; #pragma unroll
;         for (int e = 0; e < 8; ++e) { const int j = 2 * f + (e >> 2), k = e & 3; const float a = t1[e] * (rp * QSC) * C.ga[j][k], b = t2[e] * (rp * QSC) * C.gb[j][k]; o1[e] = a * C.c[j][k] - b * C.s[j][k]; o2[e] = b * C.c[j][k] + a * C.s[j][k]; }
;         qf[2][2 * f] = (int)cvt_pk4_fp8(o1[0], o1[1], o1[2], o1[3]); qf[2][2 * f + 1] = (int)cvt_pk4_fp8(o1[4], o1[5], o1[6], o1[7]);
;         qf[2][4 + 2 * f] = (int)cvt_pk4_fp8(o2[0], o2[1], o2[2], o2[3]); qf[2][5 + 2 * f] = (int)cvt_pk4_fp8(o2[4], o2[5], o2[6], o2[7]); }
	v_mov_b32_e32 v34, v28
	v_mov_b32_e32 v35, v24
	v_pk_mul_f32 v[32:33], v[34:35], v[32:33]
	v_mov_b32_e32 v34, v20
	v_mov_b32_e32 v35, v16
	v_pk_mul_f32 v[34:35], v[34:35], v[32:33]
	v_mov_b32_e32 v74, v79
	v_sub_f32_e32 v36, v35, v34
	v_mov_b32_e32 v34, v16
	v_mov_b32_e32 v35, v20
	v_pk_mul_f32 v[32:33], v[34:35], v[32:33]
	v_mov_b32_e32 v24, v29
	v_add_f32_e32 v34, v32, v33
	v_pk_mul_f32 v[32:33], v[74:75], v[96:97] op_sel_hi:[1,0]
	v_mov_b32_e32 v16, v21
	v_pk_mul_f32 v[24:25], v[24:25], v[32:33]
	v_mov_b32_e32 v20, v17
	v_pk_mul_f32 v[28:29], v[16:17], v[24:25]
	v_pk_mul_f32 v[16:17], v[20:21], v[24:25]
	v_mov_b32_e32 v20, v30
	v_add_f32_e32 v24, v16, v17
	v_mov_b32_e32 v16, v76
	v_mov_b32_e32 v17, v70
	v_pk_mul_f32 v[16:17], v[16:17], v[96:97] op_sel_hi:[1,0]
	v_mov_b32_e32 v21, v26
	v_pk_mul_f32 v[16:17], v[20:21], v[16:17]
	v_mov_b32_e32 v20, v22
	v_mov_b32_e32 v21, v18
	v_pk_mul_f32 v[20:21], v[20:21], v[16:17]
	v_mov_b32_e32 v70, v77
	v_sub_f32_e32 v25, v21, v20
	v_mov_b32_e32 v20, v18
	v_mov_b32_e32 v21, v22
	v_pk_mul_f32 v[16:17], v[20:21], v[16:17]
	v_sub_f32_e32 v28, v29, v28
	v_add_f32_e32 v29, v16, v17
	v_pk_mul_f32 v[16:17], v[70:71], v[96:97] op_sel_hi:[1,0]
	v_mov_b32_e32 v26, v31
	v_pk_mul_f32 v[16:17], v[26:27], v[16:17]
	v_mov_b32_e32 v18, v23
	v_mov_b32_e32 v22, v19
	v_pk_mul_f32 v[20:21], v[18:19], v[16:17]
	v_pk_mul_f32 v[16:17], v[22:23], v[16:17]
	v_sub_f32_e32 v20, v21, v20
	v_add_f32_e32 v21, v16, v17
	v_mov_b32_e32 v16, v72
	v_mov_b32_e32 v17, v66
	v_pk_mul_f32 v[16:17], v[16:17], v[96:97] op_sel_hi:[1,0]
	v_mov_b32_e32 v18, v12
	v_mov_b32_e32 v19, v8
	v_pk_mul_f32 v[16:17], v[18:19], v[16:17]
	v_mov_b32_e32 v18, v4
	v_mov_b32_e32 v19, v0
	v_pk_mul_f32 v[18:19], v[18:19], v[16:17]
	v_mov_b32_e32 v66, v73
	v_sub_f32_e32 v22, v19, v18
	v_mov_b32_e32 v18, v0
	v_mov_b32_e32 v19, v4
	v_pk_mul_f32 v[16:17], v[18:19], v[16:17]
	v_mov_b32_e32 v8, v13
	v_add_f32_e32 v18, v16, v17
	v_pk_mul_f32 v[16:17], v[66:67], v[96:97] op_sel_hi:[1,0]
	v_mov_b32_e32 v0, v5
	v_pk_mul_f32 v[8:9], v[8:9], v[16:17]
	v_mov_b32_e32 v4, v1
	v_pk_mul_f32 v[12:13], v[0:1], v[8:9]
	v_pk_mul_f32 v[0:1], v[4:5], v[8:9]
	v_mov_b32_e32 v4, v14
	v_add_f32_e32 v8, v0, v1
	v_mov_b32_e32 v0, v68
	v_mov_b32_e32 v1, v64
	v_pk_mul_f32 v[0:1], v[0:1], v[96:97] op_sel_hi:[1,0]
	v_mov_b32_e32 v5, v10
	v_pk_mul_f32 v[0:1], v[4:5], v[0:1]
	v_mov_b32_e32 v4, v6
	v_mov_b32_e32 v5, v2
	v_pk_mul_f32 v[4:5], v[4:5], v[0:1]
	v_cvt_pk_fp8_f32 v170, v162, v163 op_sel:[0,0,1]
	v_sub_f32_e32 v9, v5, v4
	v_mov_b32_e32 v4, v2
	v_mov_b32_e32 v5, v6
	v_sub_f32_e32 v12, v13, v12
	v_pk_mul_f32 v[0:1], v[4:5], v[0:1]
	v_mov_b32_e32 v64, v69
	v_cvt_pk_fp8_f32 v172, v142, v143
	v_cvt_pk_fp8_f32 v173, v140, v141
	v_cvt_pk_fp8_f32 v174, v134, v135
	v_cvt_pk_fp8_f32 v175, v132, v133
	v_cvt_pk_fp8_f32 v176, v126, v127
	v_cvt_pk_fp8_f32 v177, v124, v125
	v_cvt_pk_fp8_f32 v178, v118, v119
	v_cvt_pk_fp8_f32 v179, v116, v117
	v_cvt_pk_fp8_f32 v180, v110, v111
	v_cvt_pk_fp8_f32 v181, v108, v109
	v_cvt_pk_fp8_f32 v160, v94, v60
	v_cvt_pk_fp8_f32 v164, v97, v56
	v_add_f32_e32 v13, v0, v1
	v_pk_mul_f32 v[0:1], v[64:65], v[96:97] op_sel_hi:[1,0]
	v_mov_b32_e32 v10, v15
	v_cvt_pk_fp8_f32 v162, v36, v28
	v_cvt_pk_fp8_f32 v163, v22, v12
	v_cvt_pk_fp8_f32 v166, v34, v24
	v_cvt_pk_fp8_f32 v167, v18, v8
	v_pk_mul_f32 v[0:1], v[10:11], v[0:1]
	v_mov_b32_e32 v2, v7
	v_mov_b32_e32 v6, v3
	v_pk_mul_f32 v[4:5], v[2:3], v[0:1]
	v_pk_mul_f32 v[0:1], v[6:7], v[0:1]
	v_sub_f32_e32 v2, v5, v4
	v_add_f32_e32 v0, v0, v1
	v_cvt_pk_fp8_f32 v172, v138, v139 op_sel:[0,0,1]
	v_cvt_pk_fp8_f32 v173, v136, v137 op_sel:[0,0,1]
	v_cvt_pk_fp8_f32 v174, v130, v131 op_sel:[0,0,1]
	v_cvt_pk_fp8_f32 v175, v128, v129 op_sel:[0,0,1]
	v_cvt_pk_fp8_f32 v176, v122, v123 op_sel:[0,0,1]
	v_cvt_pk_fp8_f32 v177, v120, v121 op_sel:[0,0,1]
	v_cvt_pk_fp8_f32 v178, v114, v115 op_sel:[0,0,1]
	v_cvt_pk_fp8_f32 v179, v112, v113 op_sel:[0,0,1]
	v_cvt_pk_fp8_f32 v180, v106, v107 op_sel:[0,0,1]
	v_cvt_pk_fp8_f32 v181, v104, v105 op_sel:[0,0,1]
	v_cvt_pk_fp8_f32 v160, v57, v52 op_sel:[0,0,1]
	v_cvt_pk_fp8_f32 v164, v61, v53 op_sel:[0,0,1]
	v_cvt_pk_fp8_f32 v162, v25, v20 op_sel:[0,0,1]
	v_cvt_pk_fp8_f32 v163, v9, v2 op_sel:[0,0,1]
	v_cvt_pk_fp8_f32 v166, v29, v21 op_sel:[0,0,1]
	v_cvt_pk_fp8_f32 v167, v13, v0 op_sel:[0,0,1]
	s_mul_i32 s6, s0, 0x5000
	s_add_i32 s6, s6, 0
	v_bitop3_b32 v193, v193, 16, v194 bitop3:0x36
	v_add_u32_e32 v48, s6, v192
	v_add_u32_e32 v49, s6, v193
	ds_read_b128 v[16:19], v48
	ds_read_b128 v[20:23], v49
	v_mov_b64_e32 v[46:47], s[26:27]
	v_mov_b64_e32 v[44:45], s[24:25]
	v_mov_b64_e32 v[42:43], s[22:23]
	v_mov_b64_e32 v[40:41], s[20:21]
	v_mov_b64_e32 v[38:39], s[18:19]
	v_mov_b64_e32 v[36:37], s[16:17]
	v_mov_b64_e32 v[34:35], s[14:15]
	v_mov_b64_e32 v[32:33], s[12:13]
	ds_read_b128 v[50:53], v48 offset:2048
	ds_read_b128 v[54:57], v49 offset:2048
	s_waitcnt lgkmcnt(2)
	v_mfma_f32_32x32x64_f8f6f4 v[0:15], v[16:23], v[168:175], v[32:47]
	s_and_b64 vcc, exec, s[4:5]
	s_waitcnt lgkmcnt(0)
	v_mfma_f32_32x32x64_f8f6f4 v[16:31], v[50:57], v[168:175], v[32:47]
	s_nop 14
	ds_read_b128 v[36:39], v49 offset:4096
	ds_read_b128 v[32:35], v48 offset:4096
	ds_read_b128 v[40:43], v48 offset:6144
	ds_read_b128 v[44:47], v49 offset:6144
	s_waitcnt lgkmcnt(2)
	v_mfma_f32_32x32x64_f8f6f4 v[0:15], v[32:39], v[176:183], v[0:15]
	s_waitcnt lgkmcnt(0)
	v_mfma_f32_32x32x64_f8f6f4 v[16:31], v[40:47], v[176:183], v[16:31]
	ds_read_b128 v[36:39], v49 offset:8192
	ds_read_b128 v[32:35], v48 offset:8192
	ds_read_b128 v[40:43], v48 offset:10240
	ds_read_b128 v[44:47], v49 offset:10240
	s_waitcnt lgkmcnt(2)
	v_mfma_f32_32x32x64_f8f6f4 v[0:15], v[32:39], v[160:167], v[0:15]
	s_waitcnt lgkmcnt(0)
	v_mfma_f32_32x32x64_f8f6f4 v[16:31], v[40:47], v[160:167], v[16:31]
	s_nop 15
	s_nop 1
	v_max_f32_e32 v32, v1, v1
	v_max_f32_e32 v33, v0, v0
	v_max_f32_e32 v32, v33, v32
	v_max3_f32 v32, v32, v2, v3
	v_max3_f32 v32, v32, v4, v5
	v_max3_f32 v32, v32, v6, v7
	v_max3_f32 v32, v32, v8, v9
	v_max3_f32 v32, v32, v10, v11
	v_max3_f32 v32, v32, v12, v13
	v_max3_f32 v32, v32, v14, v15
	v_max3_f32 v32, v32, v16, v17
	v_max3_f32 v32, v32, v18, v19
	v_max3_f32 v32, v32, v20, v21
	v_max3_f32 v32, v32, v22, v23
	v_max3_f32 v32, v32, v24, v25
	v_max3_f32 v32, v32, v26, v27
	v_max3_f32 v32, v32, v28, v29
	v_max3_f32 v32, v32, v30, v31
	v_mov_b32_e32 v33, v32
	s_nop 1
	v_permlane32_swap_b32_e32 v32, v33
	s_cbranch_vccz .LBB0_584
	s_setprio 1
